# same epilogue: the f32 residual path waits inside its own load block; the bf16 path no longer waits for store acknowledgements before every group
# speedup vs baseline: 1.0111x; 1.0009x over previous
; __device__ __forceinline__ void st16_wt(void* p, u32x4 v) { asm volatile("global_store_dwordx4 %0, %1, off sc1\n\ts_nop 1" :: "v"(p), "v"(v) : "memory"); }
; __device__ __forceinline__ unsigned cvt_pk_bf16(float lo, float hi) { unsigned r; asm volatile("v_cvt_pk_bf16_f32 %0, %1, %2" : "=v"(r) : "v"(lo), "v"(hi)); return r; }
;     __device__ __forceinline__ void operator()(const Acc& acc, const Unit& u, int wr, int wc, int fr, int fq, const LAS float* tab) const {
;     ...
;             for (int m = 0; m < 4; ++m) {
;                 const size_t row = (size_t)u.pm * BM + ai * HALF + wr * 64 + m * 16 + fr; const size_t off = row * D + col0; float ss = 0.f;
; #pragma unroll
;                 for (int bj = 0; bj < 2; ++bj) { f32x4 b0, b1;
;                     if (base32) { b0 = __builtin_nontemporal_load((const f32x4*)(base32 + off + bj * HALF)); b1 = __builtin_nontemporal_load((const f32x4*)(base32 + off + bj * HALF + 4)); }
;                     else { const u32x4 b4 = rb[ai][m][bj];
;                         b0 = (f32x4){__uint_as_float(b4.x << 16), __uint_as_float(b4.x & 0xFFFF0000u), __uint_as_float(b4.y << 16), __uint_as_float(b4.y & 0xFFFF0000u)};
;                         b1 = (f32x4){__uint_as_float(b4.z << 16), __uint_as_float(b4.z & 0xFFFF0000u), __uint_as_float(b4.w << 16), __uint_as_float(b4.w & 0xFFFF0000u)}; }
;                     const f32x4 o0 = b0 + acc[ai][bj][m][0], o1 = b1 + acc[ai][bj][m][1];
;                     if (out32) {
;                         if (!dry) { *(f32x4*)(out32 + off + bj * HALF) = o0; *(f32x4*)(out32 + off + bj * HALF + 4) = o1; }
;                         continue; }
;                     ss += ((o0[0] * o0[0] + o0[1] * o0[1]) + (o0[2] * o0[2] + o0[3] * o0[3])) + ((o1[0] * o1[0] + o1[1] * o1[1]) + (o1[2] * o1[2] + o1[3] * o1[3]));
;                     u32x4 w; w.x = cvt_pk_bf16(o0[0], o0[1]); w.y = cvt_pk_bf16(o0[2], o0[3]); w.z = cvt_pk_bf16(o1[0], o1[1]); w.w = cvt_pk_bf16(o1[2], o1[3]);
;                     if (!dry) st16_wt(xb + off + bj * HALF, w); }
;                 if (out32) continue;
;                 ss = sum_rows4(ss);
;                 if (fq == 0 && !dry) ssp[row * 16 + u.pn * 4 + wc] = ss;
.LBB0_1864:
	v_lshlrev_b64 v[194:195], 10, v[220:221]
	v_lshl_add_u64 v[224:225], v[194:195], 0, v[218:219]
	v_cndmask_b32_e64 v194, 0, 1, s[18:19]
	s_mov_b64 s[34:35], -1
	v_cmp_ne_u32_e64 s[8:9], 1, v194
	s_andn2_b64 vcc, exec, s[18:19]
	v_lshl_add_u64 v[222:223], v[224:225], 2, s[10:11]
	s_cbranch_vccnz .LBB0_1866
	global_load_dwordx4 v[198:201], v[222:223], off offset:16 nt
	global_load_dwordx4 v[194:197], v[222:223], off nt
	global_load_dwordx4 v[244:247], v[222:223], off offset:528 nt
	global_load_dwordx4 v[248:251], v[222:223], off offset:512 nt
	s_waitcnt vmcnt(0)
	s_mov_b64 s[34:35], 0
.LBB0_1866:
	s_andn2_b64 vcc, exec, s[34:35]
	s_cbranch_vccnz .LBB0_1868
	v_lshlrev_b32_e32 v194, 16, v190
	v_and_b32_e32 v195, 0xffff0000, v190
	v_lshlrev_b32_e32 v196, 16, v191
	v_and_b32_e32 v197, 0xffff0000, v191
	v_lshlrev_b32_e32 v198, 16, v192
	v_and_b32_e32 v199, 0xffff0000, v192
	v_lshlrev_b32_e32 v200, 16, v193
	v_and_b32_e32 v201, 0xffff0000, v193
.LBB0_1868:
	v_lshl_add_u64 v[190:191], v[224:225], 1, s[14:15]
	v_pk_add_f32 v[192:193], v[164:165], v[196:197]
	v_pk_add_f32 v[196:197], v[162:163], v[194:195]
	v_pk_add_f32 v[194:195], v[160:161], v[200:201]
	v_pk_add_f32 v[198:199], v[158:159], v[198:199]
	v_cvt_pk_bf16_f32 v158, v196, v197
	v_cvt_pk_bf16_f32 v159, v192, v193
	s_and_b64 vcc, exec, s[8:9]
	v_cvt_pk_bf16_f32 v160, v198, v199
	v_cvt_pk_bf16_f32 v161, v194, v195
	s_mov_b64 s[34:35], -1
	global_store_dwordx4 v[190:191], v[158:161], off sc1
	s_nop 1
	s_cbranch_vccnz .LBB0_1870
	s_nop 1
	v_mov_b32_e32 v162, v244
	v_mov_b32_e32 v163, v245
	v_mov_b32_e32 v164, v246
	v_mov_b32_e32 v165, v247
	v_mov_b32_e32 v158, v248
	v_mov_b32_e32 v159, v249
	v_mov_b32_e32 v160, v250
	v_mov_b32_e32 v161, v251
	s_mov_b64 s[34:35], 0
.LBB0_1870:
	s_andn2_b64 vcc, exec, s[34:35]
	s_cbranch_vccnz .LBB0_1872
	v_lshlrev_b32_e32 v158, 16, v186
	v_and_b32_e32 v159, 0xffff0000, v186
	v_lshlrev_b32_e32 v160, 16, v187
	v_and_b32_e32 v161, 0xffff0000, v187
	v_lshlrev_b32_e32 v162, 16, v188
	v_and_b32_e32 v163, 0xffff0000, v188
	v_lshlrev_b32_e32 v164, 16, v189
	v_and_b32_e32 v165, 0xffff0000, v189
.LBB0_1872:
	v_pk_add_f32 v[152:153], v[152:153], v[160:161]
	v_pk_add_f32 v[150:151], v[150:151], v[158:159]
	v_mul_f32_e32 v186, v197, v197
	v_mul_f32_e32 v187, v193, v193
	v_pk_add_f32 v[158:159], v[148:149], v[164:165]
	v_pk_add_f32 v[148:149], v[146:147], v[162:163]
	v_mul_f32_e32 v146, v151, v151
	v_mul_f32_e32 v147, v153, v153
	v_fmac_f32_e32 v186, v196, v196
	v_fmac_f32_e32 v187, v192, v192
	v_fmac_f32_e32 v146, v150, v150
	v_fmac_f32_e32 v147, v152, v152
	v_add_f32_e32 v186, v186, v187
	v_mul_f32_e32 v187, v199, v199
	v_mul_f32_e32 v188, v195, v195
	s_lshl_b32 s0, s30, 2
	v_add_f32_e32 v146, v146, v147
	v_mul_f32_e32 v147, v149, v149
	v_mul_f32_e32 v160, v159, v159
	v_fmac_f32_e32 v187, v198, v198
	v_fmac_f32_e32 v188, v194, v194
	s_ashr_i32 s1, s0, 31
	v_fmac_f32_e32 v147, v148, v148
	v_fmac_f32_e32 v160, v158, v158
	v_add_f32_e32 v187, v187, v188
	s_lshl_b64 s[0:1], s[0:1], 2
	v_add_f32_e32 v147, v147, v160
	v_add_f32_e32 v186, v186, v187
	s_add_u32 s30, s53, s0
	v_add_f32_e32 v146, v146, v147
	s_addc_u32 s31, s54, s1
	v_add_f32_e32 v160, v186, v146
	v_cvt_pk_bf16_f32 v146, v150, v151
	s_mov_b64 s[0:1], 0x100
	v_cvt_pk_bf16_f32 v147, v152, v153
	v_cvt_pk_bf16_f32 v148, v148, v149
	v_cvt_pk_bf16_f32 v149, v158, v159
	v_lshl_add_u64 v[150:151], v[190:191], 0, s[0:1]
	global_store_dwordx4 v[150:151], v[146:149], off sc1
	s_nop 1
	v_mov_b32_e32 v146, v160
	s_nop 1
	v_permlane16_swap_b32_e32 v160, v146
	v_add_f32_e32 v146, v160, v146
	v_mov_b32_e32 v147, v146
	s_nop 1
	v_permlane32_swap_b32_e32 v146, v147
	s_and_saveexec_b64 s[34:35], s[4:5]
	s_cbranch_execz .LBB0_1874
	v_add_f32_e32 v148, v146, v147
	v_lshlrev_b64 v[146:147], 6, v[220:221]
	v_lshl_add_u64 v[146:147], s[30:31], 0, v[146:147]
	global_store_dword v[146:147], v148, off
.LBB0_1874:
	s_or_b64 exec, exec, s[34:35]
	v_or_b32_e32 v158, 16, v220
	v_mov_b32_e32 v159, v221
	v_lshlrev_b64 v[146:147], 10, v[158:159]
	v_lshl_add_u64 v[160:161], v[146:147], 0, v[218:219]
	s_mov_b64 s[34:35], -1
	s_and_b64 vcc, exec, s[8:9]
	v_lshl_add_u64 v[162:163], v[160:161], 2, s[10:11]
	s_cbranch_vccnz .LBB0_1876
	global_load_dwordx4 v[150:153], v[162:163], off offset:16 nt
	global_load_dwordx4 v[146:149], v[162:163], off nt
	global_load_dwordx4 v[244:247], v[162:163], off offset:528 nt
	global_load_dwordx4 v[248:251], v[162:163], off offset:512 nt
	s_waitcnt vmcnt(0)
	s_mov_b64 s[34:35], 0
.LBB0_1876:
	s_andn2_b64 vcc, exec, s[34:35]
	s_cbranch_vccnz .LBB0_1878
	v_lshlrev_b32_e32 v146, 16, v182
	v_and_b32_e32 v147, 0xffff0000, v182
	v_lshlrev_b32_e32 v148, 16, v183
	v_and_b32_e32 v149, 0xffff0000, v183
	v_lshlrev_b32_e32 v150, 16, v184
	v_and_b32_e32 v151, 0xffff0000, v184
	v_lshlrev_b32_e32 v152, 16, v185
	v_and_b32_e32 v153, 0xffff0000, v185
.LBB0_1878:
	v_lshl_add_u64 v[160:161], v[160:161], 1, s[14:15]
	v_pk_add_f32 v[148:149], v[136:137], v[148:149]
	v_pk_add_f32 v[164:165], v[134:135], v[146:147]
	v_pk_add_f32 v[146:147], v[132:133], v[152:153]
	v_pk_add_f32 v[150:151], v[130:131], v[150:151]
	v_cvt_pk_bf16_f32 v130, v164, v165
	v_cvt_pk_bf16_f32 v131, v148, v149
	s_and_b64 vcc, exec, s[8:9]
	v_cvt_pk_bf16_f32 v132, v150, v151
	v_cvt_pk_bf16_f32 v133, v146, v147
	s_mov_b64 s[34:35], -1
	global_store_dwordx4 v[160:161], v[130:133], off sc1
	s_nop 1
	s_cbranch_vccnz .LBB0_1880
	s_nop 1
	v_mov_b32_e32 v134, v244
	v_mov_b32_e32 v135, v245
	v_mov_b32_e32 v136, v246
	v_mov_b32_e32 v137, v247
	v_mov_b32_e32 v130, v248
	v_mov_b32_e32 v131, v249
	v_mov_b32_e32 v132, v250
	v_mov_b32_e32 v133, v251
	s_mov_b64 s[34:35], 0
; __device__ __forceinline__ void st16_wt(void* p, u32x4 v) { asm volatile("global_store_dwordx4 %0, %1, off sc1\n\ts_nop 1" :: "v"(p), "v"(v) : "memory"); }
; __device__ __forceinline__ unsigned cvt_pk_bf16(float lo, float hi) { unsigned r; asm volatile("v_cvt_pk_bf16_f32 %0, %1, %2" : "=v"(r) : "v"(lo), "v"(hi)); return r; }
;     __device__ __forceinline__ void operator()(const Acc& acc, const Unit& u, int wr, int wc, int fr, int fq, const LAS float* tab) const {
;     ...
;             for (int m = 0; m < 4; ++m) {
;                 const size_t row = (size_t)u.pm * BM + ai * HALF + wr * 64 + m * 16 + fr; const size_t off = row * D + col0; float ss = 0.f;
; #pragma unroll
;                 for (int bj = 0; bj < 2; ++bj) { f32x4 b0, b1;
;                     if (base32) { b0 = __builtin_nontemporal_load((const f32x4*)(base32 + off + bj * HALF)); b1 = __builtin_nontemporal_load((const f32x4*)(base32 + off + bj * HALF + 4)); }
;                     else { const u32x4 b4 = rb[ai][m][bj];
;                         b0 = (f32x4){__uint_as_float(b4.x << 16), __uint_as_float(b4.x & 0xFFFF0000u), __uint_as_float(b4.y << 16), __uint_as_float(b4.y & 0xFFFF0000u)};
;                         b1 = (f32x4){__uint_as_float(b4.z << 16), __uint_as_float(b4.z & 0xFFFF0000u), __uint_as_float(b4.w << 16), __uint_as_float(b4.w & 0xFFFF0000u)}; }
;                     const f32x4 o0 = b0 + acc[ai][bj][m][0], o1 = b1 + acc[ai][bj][m][1];
;                     if (out32) {
;                         if (!dry) { *(f32x4*)(out32 + off + bj * HALF) = o0; *(f32x4*)(out32 + off + bj * HALF + 4) = o1; }
;                         continue; }
;                     ss += ((o0[0] * o0[0] + o0[1] * o0[1]) + (o0[2] * o0[2] + o0[3] * o0[3])) + ((o1[0] * o1[0] + o1[1] * o1[1]) + (o1[2] * o1[2] + o1[3] * o1[3]));
;                     u32x4 w; w.x = cvt_pk_bf16(o0[0], o0[1]); w.y = cvt_pk_bf16(o0[2], o0[3]); w.z = cvt_pk_bf16(o1[0], o1[1]); w.w = cvt_pk_bf16(o1[2], o1[3]);
;                     if (!dry) st16_wt(xb + off + bj * HALF, w); }
;                 if (out32) continue;
;                 ss = sum_rows4(ss);
;                 if (fq == 0 && !dry) ssp[row * 16 + u.pn * 4 + wc] = ss;
.LBB0_1880:
	s_andn2_b64 vcc, exec, s[34:35]
	s_cbranch_vccnz .LBB0_1882
	v_lshlrev_b32_e32 v130, 16, v178
	v_and_b32_e32 v131, 0xffff0000, v178
	v_lshlrev_b32_e32 v132, 16, v179
	v_and_b32_e32 v133, 0xffff0000, v179
	v_lshlrev_b32_e32 v134, 16, v180
	v_and_b32_e32 v135, 0xffff0000, v180
	v_lshlrev_b32_e32 v136, 16, v181
	v_and_b32_e32 v137, 0xffff0000, v181
.LBB0_1882:
	v_pk_add_f32 v[128:129], v[128:129], v[132:133]
	v_pk_add_f32 v[126:127], v[126:127], v[130:131]
	v_mul_f32_e32 v152, v165, v165
	v_mul_f32_e32 v149, v149, v149
	v_pk_add_f32 v[130:131], v[120:121], v[136:137]
	v_pk_add_f32 v[120:121], v[118:119], v[134:135]
	v_mul_f32_e32 v118, v127, v127
	v_mul_f32_e32 v119, v129, v129
	v_fmac_f32_e32 v152, v164, v164
	v_fmac_f32_e32 v149, v148, v148
	v_fmac_f32_e32 v118, v126, v126
	v_fmac_f32_e32 v119, v128, v128
	v_add_f32_e32 v148, v152, v149
	v_mul_f32_e32 v149, v151, v151
	v_mul_f32_e32 v147, v147, v147
	v_add_f32_e32 v118, v118, v119
	v_mul_f32_e32 v119, v121, v121
	v_mul_f32_e32 v132, v131, v131
	v_fmac_f32_e32 v149, v150, v150
	v_fmac_f32_e32 v147, v146, v146
	v_fmac_f32_e32 v119, v120, v120
	v_fmac_f32_e32 v132, v130, v130
	v_add_f32_e32 v146, v149, v147
	v_add_f32_e32 v119, v119, v132
	v_add_f32_e32 v146, v148, v146
	v_add_f32_e32 v118, v118, v119
	v_add_f32_e32 v132, v146, v118
	v_cvt_pk_bf16_f32 v118, v126, v127
	v_cvt_pk_bf16_f32 v119, v128, v129
	v_cvt_pk_bf16_f32 v120, v120, v121
	v_cvt_pk_bf16_f32 v121, v130, v131
	v_lshl_add_u64 v[126:127], v[160:161], 0, s[0:1]
	global_store_dwordx4 v[126:127], v[118:121], off sc1
	s_nop 1
	v_mov_b32_e32 v118, v132
	s_nop 1
	v_permlane16_swap_b32_e32 v132, v118
	v_add_f32_e32 v118, v132, v118
	v_mov_b32_e32 v119, v118
	s_nop 1
	v_permlane32_swap_b32_e32 v118, v119
	s_and_saveexec_b64 s[34:35], s[4:5]
	s_cbranch_execz .LBB0_1884
	v_add_f32_e32 v120, v118, v119
	v_lshlrev_b64 v[118:119], 6, v[158:159]
	v_lshl_add_u64 v[118:119], s[30:31], 0, v[118:119]
	global_store_dword v[118:119], v120, off
.LBB0_1884:
	s_or_b64 exec, exec, s[34:35]
	v_or_b32_e32 v130, 32, v220
	v_mov_b32_e32 v131, v221
	v_lshlrev_b64 v[118:119], 10, v[130:131]
	v_lshl_add_u64 v[132:133], v[118:119], 0, v[218:219]
	s_mov_b64 s[34:35], -1
	s_and_b64 vcc, exec, s[8:9]
	v_lshl_add_u64 v[134:135], v[132:133], 2, s[10:11]
	s_cbranch_vccnz .LBB0_1886
	global_load_dwordx4 v[126:129], v[134:135], off offset:16 nt
	global_load_dwordx4 v[118:121], v[134:135], off nt
	global_load_dwordx4 v[244:247], v[134:135], off offset:528 nt
	global_load_dwordx4 v[248:251], v[134:135], off offset:512 nt
	s_waitcnt vmcnt(0)
	s_mov_b64 s[34:35], 0
.LBB0_1886:
	s_andn2_b64 vcc, exec, s[34:35]
	s_cbranch_vccnz .LBB0_1888
	v_lshlrev_b32_e32 v118, 16, v174
	v_and_b32_e32 v119, 0xffff0000, v174
	v_lshlrev_b32_e32 v120, 16, v175
	v_and_b32_e32 v121, 0xffff0000, v175
	v_lshlrev_b32_e32 v126, 16, v176
	v_and_b32_e32 v127, 0xffff0000, v176
	v_lshlrev_b32_e32 v128, 16, v177
	v_and_b32_e32 v129, 0xffff0000, v177
.LBB0_1888:
	v_lshl_add_u64 v[132:133], v[132:133], 1, s[14:15]
	v_pk_add_f32 v[120:121], v[112:113], v[120:121]
	v_pk_add_f32 v[136:137], v[110:111], v[118:119]
	v_pk_add_f32 v[118:119], v[108:109], v[128:129]
	v_pk_add_f32 v[126:127], v[106:107], v[126:127]
	v_cvt_pk_bf16_f32 v106, v136, v137
	v_cvt_pk_bf16_f32 v107, v120, v121
	s_and_b64 vcc, exec, s[8:9]
	v_cvt_pk_bf16_f32 v108, v126, v127
	v_cvt_pk_bf16_f32 v109, v118, v119
	s_mov_b64 s[34:35], -1
	global_store_dwordx4 v[132:133], v[106:109], off sc1
	s_nop 1
	s_cbranch_vccnz .LBB0_1890
	s_nop 1
	v_mov_b32_e32 v110, v244
	v_mov_b32_e32 v111, v245
	v_mov_b32_e32 v112, v246
	v_mov_b32_e32 v113, v247
	v_mov_b32_e32 v106, v248
	v_mov_b32_e32 v107, v249
	v_mov_b32_e32 v108, v250
	v_mov_b32_e32 v109, v251
	s_mov_b64 s[34:35], 0
.LBB0_1890:
	s_andn2_b64 vcc, exec, s[34:35]
	s_cbranch_vccnz .LBB0_1892
	v_lshlrev_b32_e32 v106, 16, v170
	v_and_b32_e32 v107, 0xffff0000, v170
	v_lshlrev_b32_e32 v108, 16, v171
	v_and_b32_e32 v109, 0xffff0000, v171
	v_lshlrev_b32_e32 v110, 16, v172
	v_and_b32_e32 v111, 0xffff0000, v172
	v_lshlrev_b32_e32 v112, 16, v173
	v_and_b32_e32 v113, 0xffff0000, v173
.LBB0_1892:
	v_pk_add_f32 v[100:101], v[100:101], v[108:109]
	v_pk_add_f32 v[98:99], v[98:99], v[106:107]
	v_mul_f32_e32 v128, v137, v137
	v_mul_f32_e32 v121, v121, v121
	v_pk_add_f32 v[106:107], v[96:97], v[112:113]
	v_pk_add_f32 v[96:97], v[94:95], v[110:111]
	v_mul_f32_e32 v94, v99, v99
	v_mul_f32_e32 v95, v101, v101
	v_fmac_f32_e32 v128, v136, v136
	v_fmac_f32_e32 v121, v120, v120
	v_fmac_f32_e32 v94, v98, v98
	v_fmac_f32_e32 v95, v100, v100
	v_add_f32_e32 v120, v128, v121
	v_mul_f32_e32 v121, v127, v127
	v_mul_f32_e32 v119, v119, v119
	v_add_f32_e32 v94, v94, v95
	v_mul_f32_e32 v95, v97, v97
	v_mul_f32_e32 v108, v107, v107
	v_fmac_f32_e32 v121, v126, v126
	v_fmac_f32_e32 v119, v118, v118
	v_fmac_f32_e32 v95, v96, v96
	v_fmac_f32_e32 v108, v106, v106
	v_add_f32_e32 v118, v121, v119
	v_add_f32_e32 v95, v95, v108
	v_add_f32_e32 v118, v120, v118
	v_add_f32_e32 v94, v94, v95
	v_add_f32_e32 v108, v118, v94
	v_cvt_pk_bf16_f32 v94, v98, v99
	v_cvt_pk_bf16_f32 v95, v100, v101
	v_cvt_pk_bf16_f32 v96, v96, v97
	v_cvt_pk_bf16_f32 v97, v106, v107
	v_lshl_add_u64 v[98:99], v[132:133], 0, s[0:1]
	global_store_dwordx4 v[98:99], v[94:97], off sc1
	s_nop 1
	v_mov_b32_e32 v94, v108
	s_nop 1
	v_permlane16_swap_b32_e32 v108, v94
	v_add_f32_e32 v94, v108, v94
	v_mov_b32_e32 v95, v94
	s_nop 1
	v_permlane32_swap_b32_e32 v94, v95
	s_and_saveexec_b64 s[34:35], s[4:5]
	s_cbranch_execz .LBB0_1894
	v_add_f32_e32 v96, v94, v95
	v_lshlrev_b64 v[94:95], 6, v[130:131]
	v_lshl_add_u64 v[94:95], s[30:31], 0, v[94:95]
	global_store_dword v[94:95], v96, off
; __device__ __forceinline__ void st16_wt(void* p, u32x4 v) { asm volatile("global_store_dwordx4 %0, %1, off sc1\n\ts_nop 1" :: "v"(p), "v"(v) : "memory"); }
; __device__ __forceinline__ unsigned cvt_pk_bf16(float lo, float hi) { unsigned r; asm volatile("v_cvt_pk_bf16_f32 %0, %1, %2" : "=v"(r) : "v"(lo), "v"(hi)); return r; }
;     __device__ __forceinline__ void operator()(const Acc& acc, const Unit& u, int wr, int wc, int fr, int fq, const LAS float* tab) const {
;     ...
;             for (int m = 0; m < 4; ++m) {
;                 const size_t row = (size_t)u.pm * BM + ai * HALF + wr * 64 + m * 16 + fr; const size_t off = row * D + col0; float ss = 0.f;
; #pragma unroll
;                 for (int bj = 0; bj < 2; ++bj) { f32x4 b0, b1;
;                     if (base32) { b0 = __builtin_nontemporal_load((const f32x4*)(base32 + off + bj * HALF)); b1 = __builtin_nontemporal_load((const f32x4*)(base32 + off + bj * HALF + 4)); }
;                     else { const u32x4 b4 = rb[ai][m][bj];
;                         b0 = (f32x4){__uint_as_float(b4.x << 16), __uint_as_float(b4.x & 0xFFFF0000u), __uint_as_float(b4.y << 16), __uint_as_float(b4.y & 0xFFFF0000u)};
;                         b1 = (f32x4){__uint_as_float(b4.z << 16), __uint_as_float(b4.z & 0xFFFF0000u), __uint_as_float(b4.w << 16), __uint_as_float(b4.w & 0xFFFF0000u)}; }
;                     const f32x4 o0 = b0 + acc[ai][bj][m][0], o1 = b1 + acc[ai][bj][m][1];
;                     if (out32) {
;                         if (!dry) { *(f32x4*)(out32 + off + bj * HALF) = o0; *(f32x4*)(out32 + off + bj * HALF + 4) = o1; }
;                         continue; }
;                     ss += ((o0[0] * o0[0] + o0[1] * o0[1]) + (o0[2] * o0[2] + o0[3] * o0[3])) + ((o1[0] * o1[0] + o1[1] * o1[1]) + (o1[2] * o1[2] + o1[3] * o1[3]));
;                     u32x4 w; w.x = cvt_pk_bf16(o0[0], o0[1]); w.y = cvt_pk_bf16(o0[2], o0[3]); w.z = cvt_pk_bf16(o1[0], o1[1]); w.w = cvt_pk_bf16(o1[2], o1[3]);
;                     if (!dry) st16_wt(xb + off + bj * HALF, w); }
;                 if (out32) continue;
;                 ss = sum_rows4(ss);
;                 if (fq == 0 && !dry) ssp[row * 16 + u.pn * 4 + wc] = ss;
.LBB0_1894:
	s_or_b64 exec, exec, s[34:35]
	v_or_b32_e32 v106, 48, v220
	v_mov_b32_e32 v107, v221
	v_lshlrev_b64 v[94:95], 10, v[106:107]
	v_lshl_add_u64 v[108:109], v[94:95], 0, v[218:219]
	s_mov_b64 s[34:35], -1
	s_and_b64 vcc, exec, s[8:9]
	v_lshl_add_u64 v[110:111], v[108:109], 2, s[10:11]
	s_cbranch_vccnz .LBB0_1896
	global_load_dwordx4 v[98:101], v[110:111], off offset:16 nt
	global_load_dwordx4 v[94:97], v[110:111], off nt
	global_load_dwordx4 v[244:247], v[110:111], off offset:528 nt
	global_load_dwordx4 v[248:251], v[110:111], off offset:512 nt
	s_waitcnt vmcnt(0)
	s_mov_b64 s[34:35], 0
.LBB0_1896:
	s_andn2_b64 vcc, exec, s[34:35]
	s_cbranch_vccnz .LBB0_1898
	v_lshlrev_b32_e32 v94, 16, v166
	v_and_b32_e32 v95, 0xffff0000, v166
	v_lshlrev_b32_e32 v96, 16, v167
	v_and_b32_e32 v97, 0xffff0000, v167
	v_lshlrev_b32_e32 v98, 16, v168
	v_and_b32_e32 v99, 0xffff0000, v168
	v_lshlrev_b32_e32 v100, 16, v169
	v_and_b32_e32 v101, 0xffff0000, v169
.LBB0_1898:
	v_lshl_add_u64 v[108:109], v[108:109], 1, s[14:15]
	v_pk_add_f32 v[96:97], v[88:89], v[96:97]
	v_pk_add_f32 v[112:113], v[86:87], v[94:95]
	v_pk_add_f32 v[94:95], v[84:85], v[100:101]
	v_pk_add_f32 v[98:99], v[82:83], v[98:99]
	v_cvt_pk_bf16_f32 v82, v112, v113
	v_cvt_pk_bf16_f32 v83, v96, v97
	s_and_b64 vcc, exec, s[8:9]
	v_cvt_pk_bf16_f32 v84, v98, v99
	v_cvt_pk_bf16_f32 v85, v94, v95
	s_mov_b64 s[34:35], -1
	global_store_dwordx4 v[108:109], v[82:85], off sc1
	s_nop 1
	s_cbranch_vccnz .LBB0_1900
	s_nop 1
	v_mov_b32_e32 v86, v244
	v_mov_b32_e32 v87, v245
	v_mov_b32_e32 v88, v246
	v_mov_b32_e32 v89, v247
	v_mov_b32_e32 v82, v248
	v_mov_b32_e32 v83, v249
	v_mov_b32_e32 v84, v250
	v_mov_b32_e32 v85, v251
	s_mov_b64 s[34:35], 0
.LBB0_1900:
	s_andn2_b64 vcc, exec, s[34:35]
	s_cbranch_vccnz .LBB0_1902
	v_lshlrev_b32_e32 v82, 16, v154
	v_and_b32_e32 v83, 0xffff0000, v154
	v_lshlrev_b32_e32 v84, 16, v155
	v_and_b32_e32 v85, 0xffff0000, v155
	v_lshlrev_b32_e32 v86, 16, v156
	v_and_b32_e32 v87, 0xffff0000, v156
	v_lshlrev_b32_e32 v88, 16, v157
	v_and_b32_e32 v89, 0xffff0000, v157
.LBB0_1902:
	v_pk_add_f32 v[76:77], v[76:77], v[84:85]
	v_pk_add_f32 v[74:75], v[74:75], v[82:83]
	v_mul_f32_e32 v100, v113, v113
	v_mul_f32_e32 v97, v97, v97
	v_pk_add_f32 v[82:83], v[72:73], v[88:89]
	v_pk_add_f32 v[72:73], v[70:71], v[86:87]
	v_mul_f32_e32 v70, v75, v75
	v_mul_f32_e32 v71, v77, v77
	v_fmac_f32_e32 v100, v112, v112
	v_fmac_f32_e32 v97, v96, v96
	v_fmac_f32_e32 v70, v74, v74
	v_fmac_f32_e32 v71, v76, v76
	v_add_f32_e32 v96, v100, v97
	v_mul_f32_e32 v97, v99, v99
	v_mul_f32_e32 v95, v95, v95
	v_add_f32_e32 v70, v70, v71
	v_mul_f32_e32 v71, v73, v73
	v_mul_f32_e32 v84, v83, v83
	v_fmac_f32_e32 v97, v98, v98
	v_fmac_f32_e32 v95, v94, v94
	v_fmac_f32_e32 v71, v72, v72
	v_fmac_f32_e32 v84, v82, v82
	v_add_f32_e32 v94, v97, v95
	v_add_f32_e32 v71, v71, v84
	v_add_f32_e32 v94, v96, v94
	v_add_f32_e32 v70, v70, v71
	v_add_f32_e32 v84, v94, v70
	v_cvt_pk_bf16_f32 v70, v74, v75
	v_cvt_pk_bf16_f32 v71, v76, v77
	v_cvt_pk_bf16_f32 v72, v72, v73
	v_cvt_pk_bf16_f32 v73, v82, v83
	v_lshl_add_u64 v[74:75], v[108:109], 0, s[0:1]
	global_store_dwordx4 v[74:75], v[70:73], off sc1
	s_nop 1
	v_mov_b32_e32 v70, v84
	s_nop 1
	v_permlane16_swap_b32_e32 v84, v70
	v_add_f32_e32 v70, v84, v70
	v_mov_b32_e32 v71, v70
	s_nop 1
	v_permlane32_swap_b32_e32 v70, v71
	s_and_saveexec_b64 s[34:35], s[4:5]
	s_cbranch_execz .LBB0_1904
	v_add_f32_e32 v72, v70, v71
	v_lshlrev_b64 v[70:71], 6, v[106:107]
	v_lshl_add_u64 v[70:71], s[30:31], 0, v[70:71]
	global_store_dword v[70:71], v72, off
.LBB0_1904:
	s_or_b64 exec, exec, s[34:35]
	v_lshl_add_u64 v[82:83], v[220:221], 0, s[90:91]
	v_lshlrev_b64 v[70:71], 10, v[82:83]
	v_lshl_add_u64 v[84:85], v[70:71], 0, v[218:219]
	s_mov_b64 s[34:35], -1
	s_and_b64 vcc, exec, s[8:9]
	v_lshl_add_u64 v[86:87], v[84:85], 2, s[10:11]
	s_cbranch_vccnz .LBB0_1906
	global_load_dwordx4 v[74:77], v[86:87], off offset:16 nt
	global_load_dwordx4 v[70:73], v[86:87], off nt
	global_load_dwordx4 v[244:247], v[86:87], off offset:528 nt
	global_load_dwordx4 v[248:251], v[86:87], off offset:512 nt
	s_waitcnt vmcnt(0)
	s_mov_b64 s[34:35], 0
.LBB0_1906:
	s_andn2_b64 vcc, exec, s[34:35]
	s_cbranch_vccnz .LBB0_1908
	v_lshlrev_b32_e32 v70, 16, v142
	v_and_b32_e32 v71, 0xffff0000, v142
	v_lshlrev_b32_e32 v72, 16, v143
	v_and_b32_e32 v73, 0xffff0000, v143
	v_lshlrev_b32_e32 v74, 16, v144
	v_and_b32_e32 v75, 0xffff0000, v144
	v_lshlrev_b32_e32 v76, 16, v145
	v_and_b32_e32 v77, 0xffff0000, v145
.LBB0_1908:
	v_lshl_add_u64 v[84:85], v[84:85], 1, s[14:15]
	v_pk_add_f32 v[72:73], v[64:65], v[72:73]
	v_pk_add_f32 v[88:89], v[62:63], v[70:71]
	v_pk_add_f32 v[70:71], v[60:61], v[76:77]
	v_pk_add_f32 v[74:75], v[58:59], v[74:75]
	v_cvt_pk_bf16_f32 v58, v88, v89
	v_cvt_pk_bf16_f32 v59, v72, v73
	s_and_b64 vcc, exec, s[8:9]
	v_cvt_pk_bf16_f32 v60, v74, v75
	v_cvt_pk_bf16_f32 v61, v70, v71
	s_mov_b64 s[34:35], -1
	global_store_dwordx4 v[84:85], v[58:61], off sc1
	s_nop 1
	s_cbranch_vccnz .LBB0_1910
	s_nop 1
	v_mov_b32_e32 v62, v244
	v_mov_b32_e32 v63, v245
	v_mov_b32_e32 v64, v246
	v_mov_b32_e32 v65, v247
	v_mov_b32_e32 v58, v248
	v_mov_b32_e32 v59, v249
	v_mov_b32_e32 v60, v250
	v_mov_b32_e32 v61, v251
	s_mov_b64 s[34:35], 0
.LBB0_1910:
	s_andn2_b64 vcc, exec, s[34:35]
	s_cbranch_vccnz .LBB0_1912
	v_lshlrev_b32_e32 v58, 16, v138
	v_and_b32_e32 v59, 0xffff0000, v138
	v_lshlrev_b32_e32 v60, 16, v139
	v_and_b32_e32 v61, 0xffff0000, v139
	v_lshlrev_b32_e32 v62, 16, v140
	v_and_b32_e32 v63, 0xffff0000, v140
	v_lshlrev_b32_e32 v64, 16, v141
	v_and_b32_e32 v65, 0xffff0000, v141
; __device__ __forceinline__ void st16_wt(void* p, u32x4 v) { asm volatile("global_store_dwordx4 %0, %1, off sc1\n\ts_nop 1" :: "v"(p), "v"(v) : "memory"); }
; __device__ __forceinline__ unsigned cvt_pk_bf16(float lo, float hi) { unsigned r; asm volatile("v_cvt_pk_bf16_f32 %0, %1, %2" : "=v"(r) : "v"(lo), "v"(hi)); return r; }
;     __device__ __forceinline__ void operator()(const Acc& acc, const Unit& u, int wr, int wc, int fr, int fq, const LAS float* tab) const {
;     ...
;             for (int m = 0; m < 4; ++m) {
;                 const size_t row = (size_t)u.pm * BM + ai * HALF + wr * 64 + m * 16 + fr; const size_t off = row * D + col0; float ss = 0.f;
; #pragma unroll
;                 for (int bj = 0; bj < 2; ++bj) { f32x4 b0, b1;
;                     if (base32) { b0 = __builtin_nontemporal_load((const f32x4*)(base32 + off + bj * HALF)); b1 = __builtin_nontemporal_load((const f32x4*)(base32 + off + bj * HALF + 4)); }
;                     else { const u32x4 b4 = rb[ai][m][bj];
;                         b0 = (f32x4){__uint_as_float(b4.x << 16), __uint_as_float(b4.x & 0xFFFF0000u), __uint_as_float(b4.y << 16), __uint_as_float(b4.y & 0xFFFF0000u)};
;                         b1 = (f32x4){__uint_as_float(b4.z << 16), __uint_as_float(b4.z & 0xFFFF0000u), __uint_as_float(b4.w << 16), __uint_as_float(b4.w & 0xFFFF0000u)}; }
;                     const f32x4 o0 = b0 + acc[ai][bj][m][0], o1 = b1 + acc[ai][bj][m][1];
;                     if (out32) {
;                         if (!dry) { *(f32x4*)(out32 + off + bj * HALF) = o0; *(f32x4*)(out32 + off + bj * HALF + 4) = o1; }
;                         continue; }
;                     ss += ((o0[0] * o0[0] + o0[1] * o0[1]) + (o0[2] * o0[2] + o0[3] * o0[3])) + ((o1[0] * o1[0] + o1[1] * o1[1]) + (o1[2] * o1[2] + o1[3] * o1[3]));
;                     u32x4 w; w.x = cvt_pk_bf16(o0[0], o0[1]); w.y = cvt_pk_bf16(o0[2], o0[3]); w.z = cvt_pk_bf16(o1[0], o1[1]); w.w = cvt_pk_bf16(o1[2], o1[3]);
;                     if (!dry) st16_wt(xb + off + bj * HALF, w); }
;                 if (out32) continue;
;                 ss = sum_rows4(ss);
;                 if (fq == 0 && !dry) ssp[row * 16 + u.pn * 4 + wc] = ss;
.LBB0_1912:
	v_pk_add_f32 v[56:57], v[56:57], v[60:61]
	v_pk_add_f32 v[54:55], v[54:55], v[58:59]
	v_mul_f32_e32 v76, v89, v89
	v_mul_f32_e32 v73, v73, v73
	v_pk_add_f32 v[58:59], v[52:53], v[64:65]
	v_pk_add_f32 v[52:53], v[50:51], v[62:63]
	v_mul_f32_e32 v50, v55, v55
	v_mul_f32_e32 v51, v57, v57
	v_fmac_f32_e32 v76, v88, v88
	v_fmac_f32_e32 v73, v72, v72
	v_fmac_f32_e32 v50, v54, v54
	v_fmac_f32_e32 v51, v56, v56
	v_add_f32_e32 v72, v76, v73
	v_mul_f32_e32 v73, v75, v75
	v_mul_f32_e32 v71, v71, v71
	v_add_f32_e32 v50, v50, v51
	v_mul_f32_e32 v51, v53, v53
	v_mul_f32_e32 v60, v59, v59
	v_fmac_f32_e32 v73, v74, v74
	v_fmac_f32_e32 v71, v70, v70
	v_fmac_f32_e32 v51, v52, v52
	v_fmac_f32_e32 v60, v58, v58
	v_add_f32_e32 v70, v73, v71
	v_add_f32_e32 v51, v51, v60
	v_add_f32_e32 v70, v72, v70
	v_add_f32_e32 v50, v50, v51
	v_add_f32_e32 v60, v70, v50
	v_cvt_pk_bf16_f32 v50, v54, v55
	v_cvt_pk_bf16_f32 v51, v56, v57
	v_cvt_pk_bf16_f32 v52, v52, v53
	v_cvt_pk_bf16_f32 v53, v58, v59
	v_lshl_add_u64 v[54:55], v[84:85], 0, s[0:1]
	global_store_dwordx4 v[54:55], v[50:53], off sc1
	s_nop 1
	v_mov_b32_e32 v50, v60
	s_nop 1
	v_permlane16_swap_b32_e32 v60, v50
	v_add_f32_e32 v50, v60, v50
	v_mov_b32_e32 v51, v50
	s_nop 1
	v_permlane32_swap_b32_e32 v50, v51
	s_and_saveexec_b64 s[34:35], s[4:5]
	s_cbranch_execz .LBB0_1914
	v_add_f32_e32 v52, v50, v51
	v_lshlrev_b64 v[50:51], 6, v[82:83]
	v_lshl_add_u64 v[50:51], s[30:31], 0, v[50:51]
	global_store_dword v[50:51], v52, off
.LBB0_1914:
	s_or_b64 exec, exec, s[34:35]
	s_mov_b64 s[0:1], 0x90
	v_lshl_add_u64 v[58:59], v[220:221], 0, s[0:1]
	v_lshlrev_b64 v[50:51], 10, v[58:59]
	v_lshl_add_u64 v[60:61], v[50:51], 0, v[218:219]
	s_mov_b64 s[34:35], -1
	s_and_b64 vcc, exec, s[8:9]
	v_lshl_add_u64 v[62:63], v[60:61], 2, s[10:11]
	s_cbranch_vccnz .LBB0_1916
	global_load_dwordx4 v[54:57], v[62:63], off offset:16 nt
	global_load_dwordx4 v[50:53], v[62:63], off nt
	global_load_dwordx4 v[244:247], v[62:63], off offset:528 nt
	global_load_dwordx4 v[248:251], v[62:63], off offset:512 nt
	s_waitcnt vmcnt(0)
	s_mov_b64 s[34:35], 0
.LBB0_1916:
	s_andn2_b64 vcc, exec, s[34:35]
	s_cbranch_vccnz .LBB0_1918
	v_lshlrev_b32_e32 v50, 16, v122
	v_and_b32_e32 v51, 0xffff0000, v122
	v_lshlrev_b32_e32 v52, 16, v123
	v_and_b32_e32 v53, 0xffff0000, v123
	v_lshlrev_b32_e32 v54, 16, v124
	v_and_b32_e32 v55, 0xffff0000, v124
	v_lshlrev_b32_e32 v56, 16, v125
	v_and_b32_e32 v57, 0xffff0000, v125
.LBB0_1918:
	v_lshl_add_u64 v[60:61], v[60:61], 1, s[14:15]
	v_pk_add_f32 v[52:53], v[48:49], v[52:53]
	v_pk_add_f32 v[64:65], v[46:47], v[50:51]
	v_pk_add_f32 v[50:51], v[44:45], v[56:57]
	v_pk_add_f32 v[54:55], v[42:43], v[54:55]
	v_cvt_pk_bf16_f32 v42, v64, v65
	v_cvt_pk_bf16_f32 v43, v52, v53
	s_and_b64 vcc, exec, s[8:9]
	v_cvt_pk_bf16_f32 v44, v54, v55
	v_cvt_pk_bf16_f32 v45, v50, v51
	s_mov_b64 s[34:35], -1
	global_store_dwordx4 v[60:61], v[42:45], off sc1
	s_nop 1
	s_cbranch_vccnz .LBB0_1920
	s_nop 1
	v_mov_b32_e32 v46, v244
	v_mov_b32_e32 v47, v245
	v_mov_b32_e32 v48, v246
	v_mov_b32_e32 v49, v247
	v_mov_b32_e32 v42, v248
	v_mov_b32_e32 v43, v249
	v_mov_b32_e32 v44, v250
	v_mov_b32_e32 v45, v251
	s_mov_b64 s[34:35], 0
.LBB0_1920:
	s_andn2_b64 vcc, exec, s[34:35]
	s_cbranch_vccnz .LBB0_1922
	v_lshlrev_b32_e32 v42, 16, v114
	v_and_b32_e32 v43, 0xffff0000, v114
	v_lshlrev_b32_e32 v44, 16, v115
	v_and_b32_e32 v45, 0xffff0000, v115
	v_lshlrev_b32_e32 v46, 16, v116
	v_and_b32_e32 v47, 0xffff0000, v116
	v_lshlrev_b32_e32 v48, 16, v117
	v_and_b32_e32 v49, 0xffff0000, v117
.LBB0_1922:
	v_pk_add_f32 v[40:41], v[40:41], v[44:45]
	v_pk_add_f32 v[38:39], v[38:39], v[42:43]
	v_mul_f32_e32 v56, v65, v65
	v_mul_f32_e32 v53, v53, v53
	v_pk_add_f32 v[42:43], v[36:37], v[48:49]
	v_pk_add_f32 v[36:37], v[34:35], v[46:47]
	v_mul_f32_e32 v34, v39, v39
	v_mul_f32_e32 v35, v41, v41
	v_fmac_f32_e32 v56, v64, v64
	v_fmac_f32_e32 v53, v52, v52
	v_fmac_f32_e32 v34, v38, v38
	v_fmac_f32_e32 v35, v40, v40
	v_add_f32_e32 v52, v56, v53
	v_mul_f32_e32 v53, v55, v55
	v_mul_f32_e32 v51, v51, v51
	v_add_f32_e32 v34, v34, v35
	v_mul_f32_e32 v35, v37, v37
	v_mul_f32_e32 v44, v43, v43
	v_fmac_f32_e32 v53, v54, v54
	v_fmac_f32_e32 v51, v50, v50
	v_fmac_f32_e32 v35, v36, v36
	v_fmac_f32_e32 v44, v42, v42
	v_add_f32_e32 v50, v53, v51
	v_add_f32_e32 v35, v35, v44
	v_add_f32_e32 v50, v52, v50
	v_add_f32_e32 v34, v34, v35
	v_add_f32_e32 v44, v50, v34
	v_cvt_pk_bf16_f32 v34, v38, v39
	s_mov_b64 s[0:1], 0x100
	v_cvt_pk_bf16_f32 v35, v40, v41
	v_cvt_pk_bf16_f32 v36, v36, v37
	v_cvt_pk_bf16_f32 v37, v42, v43
	v_lshl_add_u64 v[38:39], v[60:61], 0, s[0:1]
	global_store_dwordx4 v[38:39], v[34:37], off sc1
	s_nop 1
	v_mov_b32_e32 v34, v44
	s_nop 1
	v_permlane16_swap_b32_e32 v44, v34
	v_add_f32_e32 v34, v44, v34
	v_mov_b32_e32 v35, v34
	s_nop 1
	v_permlane32_swap_b32_e32 v34, v35
	s_and_saveexec_b64 s[34:35], s[4:5]
	s_cbranch_execz .LBB0_1924
	v_add_f32_e32 v36, v34, v35
	v_lshlrev_b64 v[34:35], 6, v[58:59]
	v_lshl_add_u64 v[34:35], s[30:31], 0, v[34:35]
	global_store_dword v[34:35], v36, off
.LBB0_1924:
	s_or_b64 exec, exec, s[34:35]
	s_mov_b64 s[0:1], 0xa0
	v_lshl_add_u64 v[42:43], v[220:221], 0, s[0:1]
	v_lshlrev_b64 v[34:35], 10, v[42:43]
	v_lshl_add_u64 v[44:45], v[34:35], 0, v[218:219]
	s_mov_b64 s[34:35], -1
	s_and_b64 vcc, exec, s[8:9]
	v_lshl_add_u64 v[46:47], v[44:45], 2, s[10:11]
	s_cbranch_vccnz .LBB0_1926
	global_load_dwordx4 v[38:41], v[46:47], off offset:16 nt
	global_load_dwordx4 v[34:37], v[46:47], off nt
	global_load_dwordx4 v[244:247], v[46:47], off offset:528 nt
	global_load_dwordx4 v[248:251], v[46:47], off offset:512 nt
	s_waitcnt vmcnt(0)
	s_mov_b64 s[34:35], 0
; __device__ __forceinline__ void st16_wt(void* p, u32x4 v) { asm volatile("global_store_dwordx4 %0, %1, off sc1\n\ts_nop 1" :: "v"(p), "v"(v) : "memory"); }
; __device__ __forceinline__ unsigned cvt_pk_bf16(float lo, float hi) { unsigned r; asm volatile("v_cvt_pk_bf16_f32 %0, %1, %2" : "=v"(r) : "v"(lo), "v"(hi)); return r; }
;     __device__ __forceinline__ void operator()(const Acc& acc, const Unit& u, int wr, int wc, int fr, int fq, const LAS float* tab) const {
;     ...
;             for (int m = 0; m < 4; ++m) {
;                 const size_t row = (size_t)u.pm * BM + ai * HALF + wr * 64 + m * 16 + fr; const size_t off = row * D + col0; float ss = 0.f;
; #pragma unroll
;                 for (int bj = 0; bj < 2; ++bj) { f32x4 b0, b1;
;                     if (base32) { b0 = __builtin_nontemporal_load((const f32x4*)(base32 + off + bj * HALF)); b1 = __builtin_nontemporal_load((const f32x4*)(base32 + off + bj * HALF + 4)); }
;                     else { const u32x4 b4 = rb[ai][m][bj];
;                         b0 = (f32x4){__uint_as_float(b4.x << 16), __uint_as_float(b4.x & 0xFFFF0000u), __uint_as_float(b4.y << 16), __uint_as_float(b4.y & 0xFFFF0000u)};
;                         b1 = (f32x4){__uint_as_float(b4.z << 16), __uint_as_float(b4.z & 0xFFFF0000u), __uint_as_float(b4.w << 16), __uint_as_float(b4.w & 0xFFFF0000u)}; }
;                     const f32x4 o0 = b0 + acc[ai][bj][m][0], o1 = b1 + acc[ai][bj][m][1];
;                     if (out32) {
;                         if (!dry) { *(f32x4*)(out32 + off + bj * HALF) = o0; *(f32x4*)(out32 + off + bj * HALF + 4) = o1; }
;                         continue; }
;                     ss += ((o0[0] * o0[0] + o0[1] * o0[1]) + (o0[2] * o0[2] + o0[3] * o0[3])) + ((o1[0] * o1[0] + o1[1] * o1[1]) + (o1[2] * o1[2] + o1[3] * o1[3]));
;                     u32x4 w; w.x = cvt_pk_bf16(o0[0], o0[1]); w.y = cvt_pk_bf16(o0[2], o0[3]); w.z = cvt_pk_bf16(o1[0], o1[1]); w.w = cvt_pk_bf16(o1[2], o1[3]);
;                     if (!dry) st16_wt(xb + off + bj * HALF, w); }
;                 if (out32) continue;
;                 ss = sum_rows4(ss);
;                 if (fq == 0 && !dry) ssp[row * 16 + u.pn * 4 + wc] = ss;
.LBB0_1926:
	s_andn2_b64 vcc, exec, s[34:35]
	s_cbranch_vccnz .LBB0_1928
	v_lshlrev_b32_e32 v34, 16, v102
	v_and_b32_e32 v35, 0xffff0000, v102
	v_lshlrev_b32_e32 v36, 16, v103
	v_and_b32_e32 v37, 0xffff0000, v103
	v_lshlrev_b32_e32 v38, 16, v104
	v_and_b32_e32 v39, 0xffff0000, v104
	v_lshlrev_b32_e32 v40, 16, v105
	v_and_b32_e32 v41, 0xffff0000, v105
.LBB0_1928:
	v_lshl_add_u64 v[44:45], v[44:45], 1, s[14:15]
	v_pk_add_f32 v[36:37], v[32:33], v[36:37]
	v_pk_add_f32 v[48:49], v[30:31], v[34:35]
	v_pk_add_f32 v[34:35], v[28:29], v[40:41]
	v_pk_add_f32 v[38:39], v[26:27], v[38:39]
	v_cvt_pk_bf16_f32 v26, v48, v49
	v_cvt_pk_bf16_f32 v27, v36, v37
	s_and_b64 vcc, exec, s[8:9]
	v_cvt_pk_bf16_f32 v28, v38, v39
	v_cvt_pk_bf16_f32 v29, v34, v35
	s_mov_b64 s[34:35], -1
	global_store_dwordx4 v[44:45], v[26:29], off sc1
	s_nop 1
	s_cbranch_vccnz .LBB0_1930
	s_nop 1
	v_mov_b32_e32 v30, v244
	v_mov_b32_e32 v31, v245
	v_mov_b32_e32 v32, v246
	v_mov_b32_e32 v33, v247
	v_mov_b32_e32 v26, v248
	v_mov_b32_e32 v27, v249
	v_mov_b32_e32 v28, v250
	v_mov_b32_e32 v29, v251
	s_mov_b64 s[34:35], 0
.LBB0_1930:
	s_andn2_b64 vcc, exec, s[34:35]
	s_cbranch_vccnz .LBB0_1932
	v_lshlrev_b32_e32 v26, 16, v90
	v_and_b32_e32 v27, 0xffff0000, v90
	v_lshlrev_b32_e32 v28, 16, v91
	v_and_b32_e32 v29, 0xffff0000, v91
	v_lshlrev_b32_e32 v30, 16, v92
	v_and_b32_e32 v31, 0xffff0000, v92
	v_lshlrev_b32_e32 v32, 16, v93
	v_and_b32_e32 v33, 0xffff0000, v93
.LBB0_1932:
	v_pk_add_f32 v[24:25], v[24:25], v[28:29]
	v_pk_add_f32 v[22:23], v[22:23], v[26:27]
	v_mul_f32_e32 v40, v49, v49
	v_mul_f32_e32 v37, v37, v37
	v_pk_add_f32 v[26:27], v[20:21], v[32:33]
	v_pk_add_f32 v[20:21], v[18:19], v[30:31]
	v_mul_f32_e32 v18, v23, v23
	v_mul_f32_e32 v19, v25, v25
	v_fmac_f32_e32 v40, v48, v48
	v_fmac_f32_e32 v37, v36, v36
	v_fmac_f32_e32 v18, v22, v22
	v_fmac_f32_e32 v19, v24, v24
	v_add_f32_e32 v36, v40, v37
	v_mul_f32_e32 v37, v39, v39
	v_mul_f32_e32 v35, v35, v35
	v_add_f32_e32 v18, v18, v19
	v_mul_f32_e32 v19, v21, v21
	v_mul_f32_e32 v28, v27, v27
	v_fmac_f32_e32 v37, v38, v38
	v_fmac_f32_e32 v35, v34, v34
	v_fmac_f32_e32 v19, v20, v20
	v_fmac_f32_e32 v28, v26, v26
	v_add_f32_e32 v34, v37, v35
	v_add_f32_e32 v19, v19, v28
	v_add_f32_e32 v34, v36, v34
	v_add_f32_e32 v18, v18, v19
	v_add_f32_e32 v28, v34, v18
	v_cvt_pk_bf16_f32 v18, v22, v23
	s_mov_b64 s[0:1], 0x100
	v_cvt_pk_bf16_f32 v19, v24, v25
	v_cvt_pk_bf16_f32 v20, v20, v21
	v_cvt_pk_bf16_f32 v21, v26, v27
	v_lshl_add_u64 v[22:23], v[44:45], 0, s[0:1]
	global_store_dwordx4 v[22:23], v[18:21], off sc1
	s_nop 1
	v_mov_b32_e32 v18, v28
	s_nop 1
	v_permlane16_swap_b32_e32 v28, v18
	v_add_f32_e32 v18, v28, v18
	v_mov_b32_e32 v19, v18
	s_nop 1
	v_permlane32_swap_b32_e32 v18, v19
	s_and_saveexec_b64 s[34:35], s[4:5]
	s_cbranch_execz .LBB0_1934
	v_add_f32_e32 v20, v18, v19
	v_lshlrev_b64 v[18:19], 6, v[42:43]
	v_lshl_add_u64 v[18:19], s[30:31], 0, v[18:19]
	global_store_dword v[18:19], v20, off
.LBB0_1934:
	s_or_b64 exec, exec, s[34:35]
	s_mov_b64 s[0:1], 0xb0
	v_lshl_add_u64 v[26:27], v[220:221], 0, s[0:1]
	v_lshlrev_b64 v[18:19], 10, v[26:27]
	v_lshl_add_u64 v[28:29], v[18:19], 0, v[218:219]
	s_mov_b64 s[34:35], -1
	s_and_b64 vcc, exec, s[8:9]
	v_lshl_add_u64 v[30:31], v[28:29], 2, s[10:11]
	s_cbranch_vccnz .LBB0_1936
	global_load_dwordx4 v[22:25], v[30:31], off offset:16 nt
	global_load_dwordx4 v[18:21], v[30:31], off nt
	global_load_dwordx4 v[244:247], v[30:31], off offset:528 nt
	global_load_dwordx4 v[248:251], v[30:31], off offset:512 nt
	s_waitcnt vmcnt(0)
	s_mov_b64 s[34:35], 0
.LBB0_1936:
	s_andn2_b64 vcc, exec, s[34:35]
	s_cbranch_vccnz .LBB0_1938
	v_lshlrev_b32_e32 v18, 16, v78
	v_and_b32_e32 v19, 0xffff0000, v78
	v_lshlrev_b32_e32 v20, 16, v79
	v_and_b32_e32 v21, 0xffff0000, v79
	v_lshlrev_b32_e32 v22, 16, v80
	v_and_b32_e32 v23, 0xffff0000, v80
	v_lshlrev_b32_e32 v24, 16, v81
	v_and_b32_e32 v25, 0xffff0000, v81
.LBB0_1938:
	v_lshl_add_u64 v[28:29], v[28:29], 1, s[14:15]
	v_pk_add_f32 v[20:21], v[16:17], v[20:21]
	v_pk_add_f32 v[32:33], v[14:15], v[18:19]
	v_pk_add_f32 v[18:19], v[12:13], v[24:25]
	v_pk_add_f32 v[22:23], v[10:11], v[22:23]
	v_cvt_pk_bf16_f32 v10, v32, v33
	v_cvt_pk_bf16_f32 v11, v20, v21
	s_and_b64 vcc, exec, s[8:9]
	v_cvt_pk_bf16_f32 v12, v22, v23
	v_cvt_pk_bf16_f32 v13, v18, v19
	s_mov_b64 s[8:9], -1
	global_store_dwordx4 v[28:29], v[10:13], off sc1
	s_nop 1
	s_cbranch_vccnz .LBB0_1940
	s_nop 1
	v_mov_b32_e32 v14, v244
	v_mov_b32_e32 v15, v245
	v_mov_b32_e32 v16, v246
	v_mov_b32_e32 v17, v247
	v_mov_b32_e32 v10, v248
	v_mov_b32_e32 v11, v249
	v_mov_b32_e32 v12, v250
	v_mov_b32_e32 v13, v251
	s_mov_b64 s[8:9], 0
.LBB0_1940:
	s_andn2_b64 vcc, exec, s[8:9]
	s_cbranch_vccnz .LBB0_1942
	v_lshlrev_b32_e32 v10, 16, v66
	v_and_b32_e32 v11, 0xffff0000, v66
	v_lshlrev_b32_e32 v12, 16, v67
	v_and_b32_e32 v13, 0xffff0000, v67
	v_lshlrev_b32_e32 v14, 16, v68
	v_and_b32_e32 v15, 0xffff0000, v68
	v_lshlrev_b32_e32 v16, 16, v69
	v_and_b32_e32 v17, 0xffff0000, v69
.LBB0_1942:
	v_pk_add_f32 v[8:9], v[8:9], v[12:13]
	v_pk_add_f32 v[6:7], v[6:7], v[10:11]
	v_mul_f32_e32 v24, v33, v33
	v_mul_f32_e32 v21, v21, v21
	v_pk_add_f32 v[10:11], v[4:5], v[16:17]
	v_pk_add_f32 v[4:5], v[2:3], v[14:15]
	v_mul_f32_e32 v2, v7, v7
	v_mul_f32_e32 v3, v9, v9
	v_fmac_f32_e32 v24, v32, v32
	v_fmac_f32_e32 v21, v20, v20
	v_fmac_f32_e32 v2, v6, v6
	v_fmac_f32_e32 v3, v8, v8
	v_add_f32_e32 v20, v24, v21
	v_mul_f32_e32 v21, v23, v23
	v_mul_f32_e32 v19, v19, v19
	v_add_f32_e32 v2, v2, v3
	v_mul_f32_e32 v3, v5, v5
	v_mul_f32_e32 v12, v11, v11
	v_fmac_f32_e32 v21, v22, v22
	v_fmac_f32_e32 v19, v18, v18
	v_fmac_f32_e32 v3, v4, v4
	v_fmac_f32_e32 v12, v10, v10
	v_add_f32_e32 v18, v21, v19
	v_add_f32_e32 v3, v3, v12
	v_add_f32_e32 v18, v20, v18
	v_add_f32_e32 v2, v2, v3
	v_add_f32_e32 v12, v18, v2
	v_cvt_pk_bf16_f32 v2, v6, v7
	s_mov_b64 s[0:1], 0x100
	v_cvt_pk_bf16_f32 v3, v8, v9
	v_cvt_pk_bf16_f32 v4, v4, v5
	v_cvt_pk_bf16_f32 v5, v10, v11
	v_lshl_add_u64 v[6:7], v[28:29], 0, s[0:1]
	global_store_dwordx4 v[6:7], v[2:5], off sc1
	s_nop 1
	v_mov_b32_e32 v2, v12
	s_nop 1
	v_permlane16_swap_b32_e32 v12, v2
	v_add_f32_e32 v2, v12, v2
	v_mov_b32_e32 v3, v2
	s_nop 1
	v_permlane32_swap_b32_e32 v2, v3
	s_and_saveexec_b64 s[8:9], s[4:5]
	s_cbranch_execz .LBB0_1944
	v_add_f32_e32 v4, v2, v3
	v_lshlrev_b64 v[2:3], 6, v[26:27]
	v_lshl_add_u64 v[2:3], s[30:31], 0, v[2:3]
	global_store_dword v[2:3], v4, off
